# baseline (speedup 1.0000x reference)
.Lagg_scatter_done:
	v_and_b32_e32 v40, 1, v0
	v_cmp_eq_u32_e32 vcc, 0, v40
	s_movk_i32 s52, 0xc4
	v_cmp_gt_u32_e64 s[60:61], s52, v2
	s_and_b64 vcc, vcc, s[60:61]
	s_and_saveexec_b64 s[60:61], vcc
	v_bfe_u32 v40, v0, 1, 1
	v_mul_u32_u24_e32 v40, 0x310, v40
	v_lshl_add_u32 v40, v2, 2, v40
	ds_write_b32 v40, v3 offset:21248
	ds_write_b32 v40, v4 offset:22816
	s_mov_b64 exec, s[60:61]
	s_waitcnt vmcnt(0) lgkmcnt(0)
	s_barrier
	v_lshrrev_b32_e32 v40, 6, v0
	s_nop 0
	v_readfirstlane_b32 s41, v40
	s_cmp_gt_u32 s41, 13
	s_cbranch_scc1 .Lagg_exit
	v_mov_b32_e32 v15, 1.0
	s_lshl_b32 s52, s3, 8
	s_add_u32 s68, s30, s52
	s_addc_u32 s69, s31, 0
	s_mul_i32 s52, s3, 0x61a800
	s_add_u32 s70, s14, s52
	s_addc_u32 s71, s15, 0
	s_mul_i32 s52, s3, 0x61a800
	s_add_u32 s48, s12, s52
	s_addc_u32 s49, s13, 0
	s_lshl_b32 s52, s3, 7
	s_add_u32 s52, s18, s52
	s_addc_u32 s53, s19, 0
	v_lshlrev_b32_e32 v40, 1, v1
	global_load_dwordx4 v[16:19], v40, s[52:53]
	global_load_dwordx4 v[20:23], v40, s[52:53] offset:16
	global_load_dword v56, v13, s[20:21] offset:0
	global_load_dword v57, v13, s[20:21] offset:16
	s_waitcnt vmcnt(0)
	v_not_b32_e32 v58, v56
	v_and_b32_e32 v59, 0x7fffffff, v56
	v_cmp_gt_i32_e32 vcc, 0, v56
	s_nop 1
	v_cndmask_b32_e32 v56, v58, v59, vcc
	v_not_b32_e32 v58, v57
	v_and_b32_e32 v59, 0x7fffffff, v57
	v_cmp_gt_i32_e32 vcc, 0, v57
	s_nop 1
	v_cndmask_b32_e32 v57, v58, v59, vcc
	v_mov_b32_e32 v46, v56
	v_add_f32_e32 v14, v56, v57
	v_mul_f32_e32 v58, 0x3c23d70a, v14
	v_max_f32_e32 v14, v14, v58
	s_cmp_eq_u32 s7, 0
	s_cbranch_scc1 .Lagg_slow_0
	s_lshl_b32 s40, s41, 4
	s_add_u32 s40, s40, 16
	s_sub_u32 s52, s41, 12
	s_lshl_b32 s52, s52, 3
	s_cmp_gt_u32 s41, 11
	s_cselect_b32 s40, s52, s40
	s_cselect_b32 s53, 1, 0
	v_bfe_u32 v63, v0, 2, 4
	v_lshrrev_b32_e32 v63, s53, v63
	v_add_u32_e32 v63, s40, v63
	v_cmp_gt_u32_e32 vcc, 0xc4, v63
	s_and_saveexec_b64 s[58:59], vcc
	s_cbranch_execz .Lagg_phasedone_0_0
	v_lshlrev_b32_e32 v63, 1, v63
	ds_read_u16 v60, v63 offset:18432
	v_lshrrev_b32_e32 v63, 2, v1
	s_waitcnt lgkmcnt(0)
	v_lshlrev_b32_e32 v61, 2, v60
	ds_read_b32 v58, v61 offset:14336
	ds_read_b32 v59, v61 offset:14340
	v_bfe_u32 v57, v0, 1, 1
	v_mul_u32_u24_e32 v57, 0x310, v57
	v_lshl_add_u32 v57, v60, 2, v57
	ds_read_b32 v57, v57 offset:21248
	v_lshl_add_u32 v61, v60, 4, v63
	v_mov_b32_e32 v45, 0
	v_mov_b32_e32 v48, 0
	v_mov_b32_e32 v49, 0
	v_mov_b32_e32 v50, 0
	v_mov_b32_e32 v51, 0
	v_mov_b32_e32 v52, 0
	v_mov_b32_e32 v53, 0
	v_mov_b32_e32 v54, 0
	v_mov_b32_e32 v55, 0
	s_waitcnt lgkmcnt(0)
	v_lshlrev_b32_e32 v41, 1, v58
	v_lshlrev_b32_e32 v42, 1, v59
	s_cmp_gt_u32 s41, 11
	s_cbranch_scc0 .Lagg_nosplit_0_0
	v_sub_u32_e32 v58, v42, v41
	v_add_u32_e32 v58, 2, v58
	v_lshrrev_b32_e32 v58, 2, v58
	v_lshl_add_u32 v58, v58, 1, v41
	v_and_b32_e32 v59, 4, v0
	v_cmp_eq_u32_e32 vcc, 0, v59
	s_nop 1
	v_cndmask_b32_e32 v42, v42, v58, vcc
	v_cndmask_b32_e32 v41, v58, v41, vcc
.Lagg_nosplit_0_0:
	v_cmp_lt_u32_e32 vcc, v41, v42
	s_and_saveexec_b64 s[64:65], vcc
	s_cbranch_execz .Lagg_listdone_0_0
	ds_read_u16 v40, v41
	v_add_u32_e32 v41, 2, v41
	s_waitcnt lgkmcnt(0)
	v_mad_u32_u16 v24, v40, s46, v1
	global_load_dwordx4 v[28:31], v24, s[48:49] offset:64
	global_load_dwordx4 v[24:27], v24, s[48:49]
	s_waitcnt lgkmcnt(0)
	v_add_f32_e32 v47, v46, v57
	v_mul_f32_e32 v56, 0x3c23d70a, v47
	v_max_f32_e32 v47, v47, v56
	v_sub_f32_e32 v43, v57, v47
	v_mul_f32_e32 v43, 0.5, v43
	v_mul_f32_e32 v44, 0xbf7d70a4, v47

.Lagg_listdone_0_0:
	s_mov_b64 exec, s[64:65]
	s_waitcnt vmcnt(0)
	s_cmp_gt_u32 s41, 11
	s_cbranch_scc0 .Lagg_nocomb_0_0
	s_nop 1
	v_mov_b32_dpp v24, v48 row_shr:4 row_mask:0xf bank_mask:0xf
	v_mov_b32_dpp v25, v49 row_shr:4 row_mask:0xf bank_mask:0xf
	v_mov_b32_dpp v26, v50 row_shr:4 row_mask:0xf bank_mask:0xf
	v_mov_b32_dpp v27, v51 row_shr:4 row_mask:0xf bank_mask:0xf
	v_mov_b32_dpp v28, v52 row_shr:4 row_mask:0xf bank_mask:0xf
	v_mov_b32_dpp v29, v53 row_shr:4 row_mask:0xf bank_mask:0xf
	v_mov_b32_dpp v30, v54 row_shr:4 row_mask:0xf bank_mask:0xf
	v_mov_b32_dpp v31, v55 row_shr:4 row_mask:0xf bank_mask:0xf
	v_mov_b32_e32 v40, 0x3c003c00
	v_add_f32_dpp v45, v45, v45 row_shr:4 row_mask:0xf bank_mask:0xf
	v_pk_fma_f16 v48, v24, v40, v48
	v_pk_fma_f16 v49, v25, v40, v49
	v_pk_fma_f16 v50, v26, v40, v50
	v_pk_fma_f16 v51, v27, v40, v51
	v_pk_fma_f16 v52, v28, v40, v52
	v_pk_fma_f16 v53, v29, v40, v53
	v_pk_fma_f16 v54, v30, v40, v54
	v_pk_fma_f16 v55, v31, v40, v55
	s_mov_b32 s60, 0xf0f0f0f0
	s_mov_b32 s61, 0xf0f0f0f0
	s_and_b64 exec, exec, s[60:61]
.Lagg_nocomb_0_0:
	ds_write_b32 v61, v48 offset:24448
	ds_write_b32 v61, v49 offset:27584
	ds_write_b32 v61, v50 offset:30720
	ds_write_b32 v61, v51 offset:33856
	ds_write_b32 v61, v52 offset:36992
	ds_write_b32 v61, v53 offset:40128
	ds_write_b32 v61, v54 offset:43264
	ds_write_b32 v61, v55 offset:46400
	ds_write_b32 v61, v45 offset:49536
.Lagg_phasedone_0_0:
	s_mov_b64 exec, s[58:59]
	s_sub_u32 s40, 11, s41
	s_lshl_b32 s40, s40, 4
	s_add_u32 s40, s40, 16
	s_sub_u32 s52, s41, 12
	s_xor_b32 s52, s52, 1
	s_lshl_b32 s52, s52, 3
	s_cmp_gt_u32 s41, 11
	s_cselect_b32 s40, s52, s40
	s_cselect_b32 s53, 1, 0
	v_bfe_u32 v63, v0, 2, 4
	v_lshrrev_b32_e32 v63, s53, v63
	v_add_u32_e32 v63, s40, v63
	v_cmp_gt_u32_e32 vcc, 0xc4, v63
	s_and_saveexec_b64 s[58:59], vcc
	s_cbranch_execz .Lagg_phasedone_0_1
	v_lshlrev_b32_e32 v63, 1, v63
	ds_read_u16 v60, v63 offset:18824
	v_lshrrev_b32_e32 v63, 2, v1
	s_waitcnt lgkmcnt(0)
	v_lshlrev_b32_e32 v61, 2, v60
	ds_read_b32 v58, v61 offset:15120
	ds_read_b32 v59, v61 offset:15124
	v_bfe_u32 v57, v0, 1, 1
	v_mul_u32_u24_e32 v57, 0x310, v57
	v_lshl_add_u32 v57, v60, 2, v57
	ds_read_b32 v57, v57 offset:21248
	v_lshl_add_u32 v61, v60, 4, v63
	v_add_u32_e32 v61, 0x6e40, v61
	v_mov_b32_e32 v45, 0
	v_mov_b32_e32 v48, 0
	v_mov_b32_e32 v49, 0
	v_mov_b32_e32 v50, 0
	v_mov_b32_e32 v51, 0
	v_mov_b32_e32 v52, 0
	v_mov_b32_e32 v53, 0
	v_mov_b32_e32 v54, 0
	v_mov_b32_e32 v55, 0
	s_waitcnt lgkmcnt(0)
	v_lshlrev_b32_e32 v41, 1, v58
	v_lshlrev_b32_e32 v42, 1, v59
	s_cmp_gt_u32 s41, 11
	s_cbranch_scc0 .Lagg_nosplit_0_1
	v_sub_u32_e32 v58, v42, v41
	v_add_u32_e32 v58, 2, v58
	v_lshrrev_b32_e32 v58, 2, v58
	v_lshl_add_u32 v58, v58, 1, v41
	v_and_b32_e32 v59, 4, v0
	v_cmp_eq_u32_e32 vcc, 0, v59
	s_nop 1
	v_cndmask_b32_e32 v42, v42, v58, vcc
	v_cndmask_b32_e32 v41, v58, v41, vcc

.Lagg_end_0:
	s_mov_b64 exec, s[58:59]
	s_mul_i32 s52, s3, 0x61a800
	s_add_u32 s52, s52, 0xc35000
	s_add_u32 s48, s12, s52
	s_addc_u32 s49, s13, 0
	s_lshl_b32 s52, s3, 7
	s_add_u32 s52, s52, 0x100
	s_add_u32 s52, s18, s52
	s_addc_u32 s53, s19, 0
	v_lshlrev_b32_e32 v40, 1, v1
	global_load_dwordx4 v[16:19], v40, s[52:53]
	global_load_dwordx4 v[20:23], v40, s[52:53] offset:16
	global_load_dword v56, v13, s[20:21] offset:32
	global_load_dword v57, v13, s[20:21] offset:48
	s_waitcnt vmcnt(0)
	v_not_b32_e32 v58, v56
	v_and_b32_e32 v59, 0x7fffffff, v56
	v_cmp_gt_i32_e32 vcc, 0, v56
	s_nop 1
	v_cndmask_b32_e32 v56, v58, v59, vcc
	v_not_b32_e32 v58, v57
	v_and_b32_e32 v59, 0x7fffffff, v57
	v_cmp_gt_i32_e32 vcc, 0, v57
	s_nop 1
	v_cndmask_b32_e32 v57, v58, v59, vcc
	v_mov_b32_e32 v46, v56
	v_add_f32_e32 v14, v56, v57
	v_mul_f32_e32 v58, 0x3c23d70a, v14
	v_max_f32_e32 v14, v14, v58
	s_cmp_eq_u32 s7, 0
	s_cbranch_scc1 .Lagg_slow_1
	s_sub_u32 s40, 11, s41
	s_lshl_b32 s40, s40, 4
	s_add_u32 s40, s40, 16
	s_sub_u32 s52, s41, 12
	s_xor_b32 s52, s52, 1
	s_lshl_b32 s52, s52, 3
	s_cmp_gt_u32 s41, 11
	s_cselect_b32 s40, s52, s40
	s_cselect_b32 s53, 1, 0
	v_bfe_u32 v63, v0, 2, 4
	v_lshrrev_b32_e32 v63, s53, v63
	v_add_u32_e32 v63, s40, v63
	v_cmp_gt_u32_e32 vcc, 0xc4, v63
	s_and_saveexec_b64 s[58:59], vcc
	s_cbranch_execz .Lagg_phasedone_1_0
	v_lshlrev_b32_e32 v63, 1, v63
	ds_read_u16 v60, v63 offset:19216
	v_lshrrev_b32_e32 v63, 2, v1
	s_waitcnt lgkmcnt(0)
	v_lshlrev_b32_e32 v61, 2, v60
	ds_read_b32 v58, v61 offset:16384
	ds_read_b32 v59, v61 offset:16388
	v_bfe_u32 v57, v0, 1, 1
	v_mul_u32_u24_e32 v57, 0x310, v57
	v_lshl_add_u32 v57, v60, 2, v57
	ds_read_b32 v57, v57 offset:22816
	v_lshl_add_u32 v61, v60, 4, v63
	v_mov_b32_e32 v45, 0
	v_mov_b32_e32 v48, 0
	v_mov_b32_e32 v49, 0
	v_mov_b32_e32 v50, 0
	v_mov_b32_e32 v51, 0
	v_mov_b32_e32 v52, 0
	v_mov_b32_e32 v53, 0
	v_mov_b32_e32 v54, 0
	v_mov_b32_e32 v55, 0
	s_waitcnt lgkmcnt(0)
	v_lshlrev_b32_e32 v41, 1, v58
	v_lshlrev_b32_e32 v42, 1, v59
	v_add_u32_e32 v41, 0x1c00, v41
	v_add_u32_e32 v42, 0x1c00, v42
	s_cmp_gt_u32 s41, 11
	s_cbranch_scc0 .Lagg_nosplit_1_0
	v_sub_u32_e32 v58, v42, v41
	v_add_u32_e32 v58, 2, v58
	v_lshrrev_b32_e32 v58, 2, v58
	v_lshl_add_u32 v58, v58, 1, v41
	v_and_b32_e32 v59, 4, v0
	v_cmp_eq_u32_e32 vcc, 0, v59
	s_nop 1
	v_cndmask_b32_e32 v42, v42, v58, vcc
	v_cndmask_b32_e32 v41, v58, v41, vcc

.Lagg_phasedone_1_0:
	s_mov_b64 exec, s[58:59]
	s_lshl_b32 s40, s41, 4
	s_add_u32 s40, s40, 16
	s_sub_u32 s52, s41, 12
	s_lshl_b32 s52, s52, 3
	s_cmp_gt_u32 s41, 11
	s_cselect_b32 s40, s52, s40
	s_cselect_b32 s53, 1, 0
	v_bfe_u32 v63, v0, 2, 4
	v_lshrrev_b32_e32 v63, s53, v63
	v_add_u32_e32 v63, s40, v63
	v_cmp_gt_u32_e32 vcc, 0xc4, v63
	s_and_saveexec_b64 s[58:59], vcc
	s_cbranch_execz .Lagg_phasedone_1_1
	v_lshlrev_b32_e32 v63, 1, v63
	ds_read_u16 v60, v63 offset:19608
	v_lshrrev_b32_e32 v63, 2, v1
	s_waitcnt lgkmcnt(0)
	v_lshlrev_b32_e32 v61, 2, v60
	ds_read_b32 v58, v61 offset:17168
	ds_read_b32 v59, v61 offset:17172
	v_bfe_u32 v57, v0, 1, 1
	v_mul_u32_u24_e32 v57, 0x310, v57
	v_lshl_add_u32 v57, v60, 2, v57
	ds_read_b32 v57, v57 offset:22816
	v_lshl_add_u32 v61, v60, 4, v63
	v_add_u32_e32 v61, 0x6e40, v61
	v_mov_b32_e32 v45, 0
	v_mov_b32_e32 v48, 0
	v_mov_b32_e32 v49, 0
	v_mov_b32_e32 v50, 0
	v_mov_b32_e32 v51, 0
	v_mov_b32_e32 v52, 0
	v_mov_b32_e32 v53, 0
	v_mov_b32_e32 v54, 0
	v_mov_b32_e32 v55, 0
	s_waitcnt lgkmcnt(0)
	v_lshlrev_b32_e32 v41, 1, v58
	v_lshlrev_b32_e32 v42, 1, v59
	v_add_u32_e32 v41, 0x1c00, v41
	v_add_u32_e32 v42, 0x1c00, v42
	s_cmp_gt_u32 s41, 11
	s_cbranch_scc0 .Lagg_nosplit_1_1
	v_sub_u32_e32 v58, v42, v41
	v_add_u32_e32 v58, 2, v58
	v_lshrrev_b32_e32 v58, 2, v58
	v_lshl_add_u32 v58, v58, 1, v41
	v_and_b32_e32 v59, 4, v0
	v_cmp_eq_u32_e32 vcc, 0, v59
	s_nop 1
	v_cndmask_b32_e32 v42, v42, v58, vcc
	v_cndmask_b32_e32 v41, v58, v41, vcc
